# all five GEMM phase prologues de-serialised (branch GEMM included) plus the retln row loop with its 8 data loads issued with the stats load; on top of stack3
# speedup vs baseline: 1.0007x; 1.0007x over previous
; #define PG8_STAGE(bufoff, gbase, voff) do { _Pragma("unroll") for (int _i = 0; _i < 2; ++_i) \
;         __builtin_amdgcn_global_load_lds((const unsigned*)((const char*)(gbase) + _i * voff##_step + (voff)), (PG8_LAS unsigned*)(lds + (bufoff) + ldsw + _i * 8192), 16, 0, 0); } while (0)
; #define PG8_WAIT_V(n) asm volatile("s_waitcnt vmcnt(" #n ")" ::: "memory")
; #define PG8_BAR __builtin_amdgcn_s_barrier()
; template <class Epi, class Sched, bool ALIGN_EPI = false, bool SP2 = false>
; __device__ __forceinline__ void gemm_phase(PG8_LAS unsigned char* lds, const Gemm g, const Sched& S, const Epi& E) {
;     ...
;     const char* cA = (const char*)S.opA(g, cur) + (size_t)cur.pm * tstepA; const char* cB = (const char*)S.opB(g, cur) + (size_t)cur.pn * tstepB;
;     S.a_ready(cur);
;     if constexpr (SP2) {
;         PG8_STAGE(PG8_SB(0, 0), cB, voffB); PG8_STAGE(PG8_SB(0, 1), cB + hstepB, voffB); PG8_STAGE(PG8_SA(0, 0), cA, voffA); PG8_STAGE(PG8_SA(0, 1), cA + hstepA, voffA);
;         if (wr == 1) PG8_BAR;
;         PG8_WAIT_V(2); PG8_BAR;
;         PG8_STAGE(PG8_SB(1, 0), cB + kstep, voffB); PG8_STAGE(PG8_SA(1, 0), cA + kstep, voffA); PG8_STAGE(PG8_SB(1, 1), cB + hstepB + kstep, voffB);
;         if (Epi::NST > 0) PG8_WAIT_V(0); else PG8_WAIT_V(6);
;         PG8_BAR;
.LBB0_580:
	v_bfe_u32 v14, v12, 4, 2
	v_and_b32_e32 v13, 15, v12
	v_lshlrev_b32_e32 v15, 3, v14
	v_lshlrev_b32_e32 v14, 4, v14
	v_lshlrev_b32_e32 v12, 2, v12
	s_and_b32 s2, s2, 3
	v_lshl_or_b32 v3, s3, 6, v13
	v_lshl_or_b32 v13, v13, 6, v14
	s_lshl_b32 s3, s3, 13
	v_and_b32_e32 v12, 32, v12
	v_bitop3_b32 v16, v13, s3, v12 bitop3:0xde
	s_lshl_b32 s3, s2, 12
	v_bitop3_b32 v219, v13, s3, v12 bitop3:0xde
	v_lshl_add_u64 v[12:13], v[4:5], 0, s[78:79]
	s_add_i32 m0, s23, 0x18000
	s_nop 0
	global_load_lds_dwordx4 v[12:13], off
	v_lshl_add_u64 v[4:5], v[4:5], 0, s[84:85]
	s_add_i32 m0, s23, 0x1a000
	s_add_i32 s27, s23, 0x8000
	global_load_lds_dwordx4 v[4:5], off
	v_lshl_add_u64 v[4:5], v[6:7], 0, s[78:79]
	s_mov_b32 m0, s27
	s_add_i32 s28, s23, 0xa000
	v_readlane_b32 s4, v255, 5
	global_load_lds_dwordx4 v[4:5], off
	v_lshl_add_u64 v[4:5], v[6:7], 0, s[92:93]
	s_mov_b32 m0, s28
	v_readlane_b32 s5, v255, 6
	global_load_lds_dwordx4 v[4:5], off
	s_nop 0
	v_lshl_add_u64 v[4:5], s[4:5], 0, v[194:195]
	s_add_i32 m0, s23, 0x1c000
	v_lshl_or_b32 v220, s2, 5, v15
	global_load_lds_dwordx4 v[4:5], off
	v_lshl_add_u64 v[4:5], v[4:5], 0, s[90:91]
	s_add_i32 m0, s23, 0x1e000
	s_cmpk_lt_u32 s0, 0x100
	global_load_lds_dwordx4 v[4:5], off
	s_waitcnt vmcnt(8)
	s_barrier
	v_lshl_or_b32 v4, s2, 6, v14
	v_readlane_b32 s2, v255, 21
	v_mov_b32_e32 v5, v2
	v_readlane_b32 s3, v255, 22
	s_movk_i32 s0, 0x840
	s_waitcnt vmcnt(6)
	v_readlane_b32 s8, v255, 3
	v_lshl_add_u64 v[198:199], s[2:3], 0, v[4:5]
	v_lshrrev_b32_e32 v5, 1, v9
	v_mul_lo_u32 v4, v8, s0
	s_mov_b32 s0, 0x8400
	v_mad_u64_u32 v[4:5], s[2:3], v5, s0, v[4:5]
	v_or_b32_e32 v4, v4, v10
	v_readlane_b32 s20, v254, 63
	s_cselect_b64 s[12:13], -1, 0
	v_add_lshl_u32 v200, v4, v11, 1
	v_mov_b32_e32 v201, v2
	s_mov_b32 s0, 0
	v_add_u32_e32 v221, 0, v16
	v_readlane_b32 s30, v254, 12
	v_readlane_b32 s31, v254, 37
	v_readlane_b32 s9, v255, 4
	v_readlane_b32 s21, v255, 0
	s_mov_b32 s2, 0
	s_barrier
	s_branch .LBB0_583
